# t2 + W_in first-K-iteration vmcnt waits tolerate the 16 epilogue stores (units 2..) + dilated LDS fragment reads issued 5 MFMAs ahead from a 6-quad pool
# baseline (speedup 1.0000x reference)
.Lwin_rx0:
	s_cmp_lt_u32 s55, 2
	s_cbranch_scc1 .Lwin_ry0
	s_waitcnt vmcnt(24)
	s_branch .Lwin_rd0
.Lwin_ry0:
	s_waitcnt vmcnt(8)
	s_branch .Lwin_rd0

.LBB0_234:
	s_add_u32 s38, s0, 0xfffc0080
	s_addc_u32 s39, s1, -1
	s_add_i32 s63, 0, 0x10000
	s_cmp_eq_u32 s62, 12
	s_cselect_b32 s41, s25, s39
	s_cselect_b32 s40, s58, s38
	s_cselect_b32 s39, s27, s61
	s_cselect_b32 s38, s59, s60
	s_add_i32 s66, 0, 0x14000
	v_add_u32_e32 v134, s63, v165
	v_add_u32_e32 v160, s66, v165
	ds_read_b128 v[114:117], v134
	ds_read_b128 v[118:121], v134 offset:1024
	ds_read_b128 v[130:133], v134 offset:2048
	ds_read_b128 v[134:137], v134 offset:3072
	ds_read_b128 v[170:173], v160
	ds_read_b128 v[174:177], v160 offset:1024
	ds_read_b128 v[200:203], v160 offset:2048
	ds_read_b128 v[204:207], v160 offset:3072
	v_lshl_add_u64 v[160:161], s[0:1], 0, v[158:159]
	s_add_i32 m0, s37, 0xc000
	ds_read_b128 v[208:211], v168
	ds_read_b128 v[212:215], v168 offset:1024
	ds_read_b128 v[216:219], v168 offset:2048
	ds_read_b128 v[220:223], v168 offset:3072
	ds_read_b128 v[224:227], v168 offset:4096
	ds_read_b128 v[228:231], v168 offset:5120
	ds_read_b128 v[232:235], v168 offset:6144
	ds_read_b128 v[236:239], v168 offset:7168
	global_load_lds_dwordx4 v[160:161], off
	v_lshl_add_u64 v[160:161], s[0:1], 0, v[156:157]
	s_add_i32 m0, s37, 0xe000
	s_nop 0
	global_load_lds_dwordx4 v[160:161], off
	s_cmp_eq_u32 s62, -2
	s_cbranch_scc1 .Lwin_rx0
	s_waitcnt vmcnt(8)
.Lwin_rd0:
	s_waitcnt lgkmcnt(0)
	s_barrier
	s_setprio 1
	s_waitcnt lgkmcnt(0)
	v_mfma_f32_16x16x32_bf16 v[142:145], v[114:117], v[208:211], v[142:145]
	v_mfma_f32_16x16x32_bf16 v[138:141], v[130:133], v[208:211], v[138:141]
	v_mfma_f32_16x16x32_bf16 v[110:113], v[114:117], v[216:219], v[110:113]
	v_mfma_f32_16x16x32_bf16 v[106:109], v[130:133], v[216:219], v[106:109]
	v_mfma_f32_16x16x32_bf16 v[94:97], v[114:117], v[224:227], v[94:97]
	v_mfma_f32_16x16x32_bf16 v[90:93], v[130:133], v[224:227], v[90:93]
	v_mfma_f32_16x16x32_bf16 v[78:81], v[114:117], v[232:235], v[78:81]
	v_mfma_f32_16x16x32_bf16 v[74:77], v[130:133], v[232:235], v[74:77]
	v_mfma_f32_16x16x32_bf16 v[142:145], v[118:121], v[212:215], v[142:145]
	v_mfma_f32_16x16x32_bf16 v[138:141], v[134:137], v[212:215], v[138:141]
	v_mfma_f32_16x16x32_bf16 v[110:113], v[118:121], v[220:223], v[110:113]
	v_mfma_f32_16x16x32_bf16 v[106:109], v[134:137], v[220:223], v[106:109]
	v_mfma_f32_16x16x32_bf16 v[94:97], v[118:121], v[228:231], v[94:97]
	v_mfma_f32_16x16x32_bf16 v[90:93], v[134:137], v[228:231], v[90:93]
	v_mfma_f32_16x16x32_bf16 v[78:81], v[118:121], v[236:239], v[78:81]
	v_mfma_f32_16x16x32_bf16 v[74:77], v[134:137], v[236:239], v[74:77]
	s_setprio 0
	s_setprio 1
	v_mfma_f32_16x16x32_bf16 v[126:129], v[170:173], v[208:211], v[126:129]
	v_mfma_f32_16x16x32_bf16 v[122:125], v[200:203], v[208:211], v[122:125]
	v_mfma_f32_16x16x32_bf16 v[102:105], v[170:173], v[216:219], v[102:105]
	v_mfma_f32_16x16x32_bf16 v[98:101], v[200:203], v[216:219], v[98:101]
	v_mfma_f32_16x16x32_bf16 v[86:89], v[170:173], v[224:227], v[86:89]
	v_mfma_f32_16x16x32_bf16 v[82:85], v[200:203], v[224:227], v[82:85]
	v_mfma_f32_16x16x32_bf16 v[70:73], v[170:173], v[232:235], v[70:73]
	v_mfma_f32_16x16x32_bf16 v[66:69], v[200:203], v[232:235], v[66:69]
	v_mfma_f32_16x16x32_bf16 v[126:129], v[174:177], v[212:215], v[126:129]
	v_mfma_f32_16x16x32_bf16 v[122:125], v[204:207], v[212:215], v[122:125]
	v_mfma_f32_16x16x32_bf16 v[102:105], v[174:177], v[220:223], v[102:105]
	v_mfma_f32_16x16x32_bf16 v[98:101], v[204:207], v[220:223], v[98:101]
	v_mfma_f32_16x16x32_bf16 v[86:89], v[174:177], v[228:231], v[86:89]
	v_mfma_f32_16x16x32_bf16 v[82:85], v[204:207], v[228:231], v[82:85]
	v_mfma_f32_16x16x32_bf16 v[70:73], v[174:177], v[236:239], v[70:73]
	v_mfma_f32_16x16x32_bf16 v[66:69], v[204:207], v[236:239], v[66:69]
	s_setprio 0
	s_barrier
	s_add_i32 s63, s63, s42
	v_lshl_add_u64 v[160:161], s[38:39], 0, v[146:147]
	s_mov_b32 m0, s63
	ds_read_b128 v[208:211], v168 offset:16384
	ds_read_b128 v[212:215], v168 offset:17408
	ds_read_b128 v[216:219], v168 offset:18432
	ds_read_b128 v[220:223], v168 offset:19456
	ds_read_b128 v[224:227], v168 offset:20480
	ds_read_b128 v[228:231], v168 offset:21504
	ds_read_b128 v[232:235], v168 offset:22528
	ds_read_b128 v[236:239], v168 offset:23552
	global_load_lds_dwordx4 v[160:161], off
	s_add_i32 m0, s63, 0x2000
	s_add_u32 s64, s38, 0x40000
	v_lshl_add_u64 v[178:179], s[38:39], 0, v[148:149]
	s_addc_u32 s65, s39, 0
	s_add_i32 s63, s66, s42
	global_load_lds_dwordx4 v[178:179], off
	v_lshl_add_u64 v[240:241], s[64:65], 0, v[146:147]
	s_mov_b32 m0, s63
	v_lshl_add_u64 v[242:243], s[40:41], 0, v[148:149]
	global_load_lds_dwordx4 v[240:241], off
	v_lshl_add_u64 v[240:241], s[64:65], 0, v[148:149]
	s_add_i32 m0, s63, 0x2000
	s_nop 0
	global_load_lds_dwordx4 v[240:241], off
	v_lshl_add_u64 v[240:241], s[40:41], 0, v[146:147]
	s_mov_b32 m0, s37
	s_nop 0
	global_load_lds_dwordx4 v[240:241], off
	s_mov_b32 m0, s47
	s_nop 0
	global_load_lds_dwordx4 v[242:243], off
	s_cmp_eq_u32 s62, -2
	s_cbranch_scc1 .Lwin_rx1
	s_waitcnt vmcnt(8)
.Lwin_rd1:
	s_waitcnt lgkmcnt(0)
	s_barrier
	s_setprio 1
	s_waitcnt lgkmcnt(0)
	v_mfma_f32_16x16x32_bf16 v[62:65], v[114:117], v[208:211], v[62:65]
	v_mfma_f32_16x16x32_bf16 v[58:61], v[130:133], v[208:211], v[58:61]
	v_mfma_f32_16x16x32_bf16 v[46:49], v[114:117], v[216:219], v[46:49]
	v_mfma_f32_16x16x32_bf16 v[42:45], v[130:133], v[216:219], v[42:45]
	v_mfma_f32_16x16x32_bf16 v[30:33], v[114:117], v[224:227], v[30:33]
	v_mfma_f32_16x16x32_bf16 v[26:29], v[130:133], v[224:227], v[26:29]
	v_mfma_f32_16x16x32_bf16 v[14:17], v[114:117], v[232:235], v[14:17]
	v_mfma_f32_16x16x32_bf16 v[10:13], v[130:133], v[232:235], v[10:13]
	v_mfma_f32_16x16x32_bf16 v[62:65], v[118:121], v[212:215], v[62:65]
	v_mfma_f32_16x16x32_bf16 v[58:61], v[134:137], v[212:215], v[58:61]
	v_mfma_f32_16x16x32_bf16 v[46:49], v[118:121], v[220:223], v[46:49]
	v_mfma_f32_16x16x32_bf16 v[42:45], v[134:137], v[220:223], v[42:45]
	v_mfma_f32_16x16x32_bf16 v[30:33], v[118:121], v[228:231], v[30:33]
	v_mfma_f32_16x16x32_bf16 v[26:29], v[134:137], v[228:231], v[26:29]
	v_mfma_f32_16x16x32_bf16 v[14:17], v[118:121], v[236:239], v[14:17]
	v_mfma_f32_16x16x32_bf16 v[10:13], v[134:137], v[236:239], v[10:13]
	s_setprio 0
	s_setprio 1
	v_mfma_f32_16x16x32_bf16 v[54:57], v[170:173], v[208:211], v[54:57]
	v_mfma_f32_16x16x32_bf16 v[50:53], v[200:203], v[208:211], v[50:53]
	v_mfma_f32_16x16x32_bf16 v[38:41], v[170:173], v[216:219], v[38:41]
	v_mfma_f32_16x16x32_bf16 v[34:37], v[200:203], v[216:219], v[34:37]
	v_mfma_f32_16x16x32_bf16 v[22:25], v[170:173], v[224:227], v[22:25]
	v_mfma_f32_16x16x32_bf16 v[18:21], v[200:203], v[224:227], v[18:21]
	v_mfma_f32_16x16x32_bf16 v[6:9], v[170:173], v[232:235], v[6:9]
	v_mfma_f32_16x16x32_bf16 v[2:5], v[200:203], v[232:235], v[2:5]
	v_mfma_f32_16x16x32_bf16 v[54:57], v[174:177], v[212:215], v[54:57]
	v_mfma_f32_16x16x32_bf16 v[50:53], v[204:207], v[212:215], v[50:53]
	v_mfma_f32_16x16x32_bf16 v[38:41], v[174:177], v[220:223], v[38:41]
	v_mfma_f32_16x16x32_bf16 v[34:37], v[204:207], v[220:223], v[34:37]
	v_mfma_f32_16x16x32_bf16 v[22:25], v[174:177], v[228:231], v[22:25]
	v_mfma_f32_16x16x32_bf16 v[18:21], v[204:207], v[228:231], v[18:21]
	v_mfma_f32_16x16x32_bf16 v[6:9], v[174:177], v[236:239], v[6:9]
	v_mfma_f32_16x16x32_bf16 v[2:5], v[204:207], v[236:239], v[2:5]
	s_setprio 0
	s_barrier
	s_add_i32 s63, 0, 0x18000
	s_add_i32 s64, 0, 0x1c000
	v_add_u32_e32 v134, s63, v165
	v_add_u32_e32 v162, s64, v165
	ds_read_b128 v[114:117], v134
	ds_read_b128 v[118:121], v134 offset:1024
	ds_read_b128 v[130:133], v134 offset:2048
	ds_read_b128 v[134:137], v134 offset:3072
	ds_read_b128 v[170:173], v162
	ds_read_b128 v[174:177], v162 offset:1024
	ds_read_b128 v[200:203], v162 offset:2048
	ds_read_b128 v[204:207], v162 offset:3072
	s_add_u32 s40, s40, 0x40000
	s_addc_u32 s41, s41, 0
	s_mov_b32 m0, s48
	v_lshl_add_u64 v[244:245], s[40:41], 0, v[146:147]
	ds_read_b128 v[208:211], v168 offset:32768
	ds_read_b128 v[212:215], v168 offset:33792
	ds_read_b128 v[216:219], v168 offset:34816
	ds_read_b128 v[220:223], v168 offset:35840
	ds_read_b128 v[224:227], v168 offset:36864
	ds_read_b128 v[228:231], v168 offset:37888
	ds_read_b128 v[232:235], v168 offset:38912
	ds_read_b128 v[236:239], v168 offset:39936
	global_load_lds_dwordx4 v[244:245], off
	v_lshl_add_u64 v[244:245], s[40:41], 0, v[148:149]
	s_mov_b32 m0, s49
	s_nop 0
	global_load_lds_dwordx4 v[244:245], off
	s_waitcnt vmcnt(8)
	s_waitcnt lgkmcnt(0)
	s_barrier
	s_setprio 1
	s_waitcnt lgkmcnt(0)
	v_mfma_f32_16x16x32_bf16 v[142:145], v[114:117], v[208:211], v[142:145]
	v_mfma_f32_16x16x32_bf16 v[138:141], v[130:133], v[208:211], v[138:141]
	v_mfma_f32_16x16x32_bf16 v[110:113], v[114:117], v[216:219], v[110:113]
	v_mfma_f32_16x16x32_bf16 v[106:109], v[130:133], v[216:219], v[106:109]
	v_mfma_f32_16x16x32_bf16 v[94:97], v[114:117], v[224:227], v[94:97]
	v_mfma_f32_16x16x32_bf16 v[90:93], v[130:133], v[224:227], v[90:93]
	v_mfma_f32_16x16x32_bf16 v[78:81], v[114:117], v[232:235], v[78:81]
	v_mfma_f32_16x16x32_bf16 v[74:77], v[130:133], v[232:235], v[74:77]
	v_mfma_f32_16x16x32_bf16 v[142:145], v[118:121], v[212:215], v[142:145]
	v_mfma_f32_16x16x32_bf16 v[138:141], v[134:137], v[212:215], v[138:141]
	v_mfma_f32_16x16x32_bf16 v[110:113], v[118:121], v[220:223], v[110:113]
	v_mfma_f32_16x16x32_bf16 v[106:109], v[134:137], v[220:223], v[106:109]
	v_mfma_f32_16x16x32_bf16 v[94:97], v[118:121], v[228:231], v[94:97]
	v_mfma_f32_16x16x32_bf16 v[90:93], v[134:137], v[228:231], v[90:93]
	v_mfma_f32_16x16x32_bf16 v[78:81], v[118:121], v[236:239], v[78:81]
	v_mfma_f32_16x16x32_bf16 v[74:77], v[134:137], v[236:239], v[74:77]
	s_setprio 0
	s_setprio 1
	v_mfma_f32_16x16x32_bf16 v[126:129], v[170:173], v[208:211], v[126:129]
	v_mfma_f32_16x16x32_bf16 v[122:125], v[200:203], v[208:211], v[122:125]
	v_mfma_f32_16x16x32_bf16 v[102:105], v[170:173], v[216:219], v[102:105]
	v_mfma_f32_16x16x32_bf16 v[98:101], v[200:203], v[216:219], v[98:101]
	v_mfma_f32_16x16x32_bf16 v[86:89], v[170:173], v[224:227], v[86:89]
	v_mfma_f32_16x16x32_bf16 v[82:85], v[200:203], v[224:227], v[82:85]
	v_mfma_f32_16x16x32_bf16 v[70:73], v[170:173], v[232:235], v[70:73]
	v_mfma_f32_16x16x32_bf16 v[66:69], v[200:203], v[232:235], v[66:69]
	v_mfma_f32_16x16x32_bf16 v[126:129], v[174:177], v[212:215], v[126:129]
	v_mfma_f32_16x16x32_bf16 v[122:125], v[204:207], v[212:215], v[122:125]
	v_mfma_f32_16x16x32_bf16 v[102:105], v[174:177], v[220:223], v[102:105]
	v_mfma_f32_16x16x32_bf16 v[98:101], v[204:207], v[220:223], v[98:101]
	v_mfma_f32_16x16x32_bf16 v[86:89], v[174:177], v[228:231], v[86:89]
	v_mfma_f32_16x16x32_bf16 v[82:85], v[204:207], v[228:231], v[82:85]
	v_mfma_f32_16x16x32_bf16 v[70:73], v[174:177], v[236:239], v[70:73]
	v_mfma_f32_16x16x32_bf16 v[66:69], v[204:207], v[236:239], v[66:69]
	s_setprio 0
	s_barrier
	s_add_i32 s40, s63, s42
	v_lshl_add_u64 v[160:161], v[160:161], 0, s[90:91]
	s_mov_b32 m0, s40
	ds_read_b128 v[208:211], v168 offset:49152
	ds_read_b128 v[212:215], v168 offset:50176
	ds_read_b128 v[216:219], v168 offset:51200
	ds_read_b128 v[220:223], v168 offset:52224
	ds_read_b128 v[224:227], v168 offset:53248
	ds_read_b128 v[228:231], v168 offset:54272
	ds_read_b128 v[232:235], v168 offset:55296
	ds_read_b128 v[236:239], v168 offset:56320
	global_load_lds_dwordx4 v[160:161], off
	s_add_i32 m0, s40, 0x2000
	s_add_u32 s38, s38, 0x40080
	v_lshl_add_u64 v[160:161], v[178:179], 0, s[90:91]
	s_addc_u32 s39, s39, 0
	s_add_i32 s40, s64, s42
	global_load_lds_dwordx4 v[160:161], off
	v_lshl_add_u64 v[160:161], s[38:39], 0, v[146:147]
	s_mov_b32 m0, s40
	s_nop 0
	global_load_lds_dwordx4 v[160:161], off
	v_lshl_add_u64 v[160:161], s[38:39], 0, v[148:149]
	s_add_i32 m0, s40, 0x2000
	s_nop 0
	global_load_lds_dwordx4 v[160:161], off
	v_lshl_add_u64 v[160:161], v[240:241], 0, s[90:91]
	s_mov_b32 m0, s52
	s_nop 0
	global_load_lds_dwordx4 v[160:161], off
	v_lshl_add_u64 v[160:161], v[242:243], 0, s[90:91]
	s_mov_b32 m0, s53
	s_nop 0
	global_load_lds_dwordx4 v[160:161], off
	s_waitcnt vmcnt(8)
	s_waitcnt lgkmcnt(0)
	s_barrier
	s_setprio 1
	s_waitcnt lgkmcnt(0)
	v_mfma_f32_16x16x32_bf16 v[62:65], v[114:117], v[208:211], v[62:65]
	v_mfma_f32_16x16x32_bf16 v[58:61], v[130:133], v[208:211], v[58:61]
	v_mfma_f32_16x16x32_bf16 v[46:49], v[114:117], v[216:219], v[46:49]
	v_mfma_f32_16x16x32_bf16 v[42:45], v[130:133], v[216:219], v[42:45]
	v_mfma_f32_16x16x32_bf16 v[30:33], v[114:117], v[224:227], v[30:33]
	v_mfma_f32_16x16x32_bf16 v[26:29], v[130:133], v[224:227], v[26:29]
	v_mfma_f32_16x16x32_bf16 v[14:17], v[114:117], v[232:235], v[14:17]
	v_mfma_f32_16x16x32_bf16 v[10:13], v[130:133], v[232:235], v[10:13]
	v_mfma_f32_16x16x32_bf16 v[62:65], v[118:121], v[212:215], v[62:65]
	v_mfma_f32_16x16x32_bf16 v[58:61], v[134:137], v[212:215], v[58:61]
	v_mfma_f32_16x16x32_bf16 v[46:49], v[118:121], v[220:223], v[46:49]
	v_mfma_f32_16x16x32_bf16 v[42:45], v[134:137], v[220:223], v[42:45]
	v_mfma_f32_16x16x32_bf16 v[30:33], v[118:121], v[228:231], v[30:33]
	v_mfma_f32_16x16x32_bf16 v[26:29], v[134:137], v[228:231], v[26:29]
	v_mfma_f32_16x16x32_bf16 v[14:17], v[118:121], v[236:239], v[14:17]
	v_mfma_f32_16x16x32_bf16 v[10:13], v[134:137], v[236:239], v[10:13]
	s_setprio 0
	s_setprio 1
	v_mfma_f32_16x16x32_bf16 v[54:57], v[170:173], v[208:211], v[54:57]
	v_mfma_f32_16x16x32_bf16 v[50:53], v[200:203], v[208:211], v[50:53]
	v_mfma_f32_16x16x32_bf16 v[38:41], v[170:173], v[216:219], v[38:41]
	v_mfma_f32_16x16x32_bf16 v[34:37], v[200:203], v[216:219], v[34:37]
	v_mfma_f32_16x16x32_bf16 v[22:25], v[170:173], v[224:227], v[22:25]
	v_mfma_f32_16x16x32_bf16 v[18:21], v[200:203], v[224:227], v[18:21]
	v_mfma_f32_16x16x32_bf16 v[6:9], v[170:173], v[232:235], v[6:9]
	v_mfma_f32_16x16x32_bf16 v[2:5], v[200:203], v[232:235], v[2:5]
	v_mfma_f32_16x16x32_bf16 v[54:57], v[174:177], v[212:215], v[54:57]
	v_mfma_f32_16x16x32_bf16 v[50:53], v[204:207], v[212:215], v[50:53]
	v_mfma_f32_16x16x32_bf16 v[38:41], v[174:177], v[220:223], v[38:41]
	v_mfma_f32_16x16x32_bf16 v[34:37], v[204:207], v[220:223], v[34:37]
	v_mfma_f32_16x16x32_bf16 v[22:25], v[174:177], v[228:231], v[22:25]
	v_mfma_f32_16x16x32_bf16 v[18:21], v[204:207], v[228:231], v[18:21]
	v_mfma_f32_16x16x32_bf16 v[6:9], v[174:177], v[236:239], v[6:9]
	v_mfma_f32_16x16x32_bf16 v[2:5], v[204:207], v[236:239], v[2:5]
	s_setprio 0
	s_barrier
	s_add_i32 s62, s62, 2
	s_add_u32 s60, s60, 0x100
	s_addc_u32 s61, s61, 0
	s_add_u32 s0, s0, 0x100
	s_addc_u32 s1, s1, 0
	s_cmp_lt_u32 s62, 14
	s_cbranch_scc1 .LBB0_234
	s_andn2_b64 vcc, exec, s[22:23]
	s_cbranch_vccnz .LBB0_237
	s_barrier

.LBB0_406:
	v_add_u32_e32 v252, 0x1000, v171
	v_add_u32_e32 v253, 0x1000, v169
	s_ashr_i32 s33, s79, 8
	s_mov_b32 s3, s72
	s_mul_hi_i32 s72, s33, 0x55555556
	s_lshr_b32 s73, s72, 31
	s_add_i32 s83, s72, s73
	s_mul_i32 s72, s83, 3
	s_sub_i32 s92, s33, s72
	s_and_b32 s33, s71, 56
	s_add_i32 s72, s33, s83
	s_lshl_b32 s33, s92, 1
	s_lshr_b32 s74, 32, s33
	s_bfe_u32 s73, s79, 0x50003
	s_sub_i32 s75, 5, s33
	s_add_i32 s74, s74, -1
	s_lshr_b32 s80, s73, s75
	s_and_b32 s73, s74, s73
	s_lshl_b32 s81, s73, 8
	s_add_i32 s81, s81, s78
	v_or_b32_e32 v2, s81, v165
	v_lshlrev_b32_e32 v2, s33, v2
	s_ashr_i32 s73, s72, 31
	v_add_u32_e32 v152, s80, v2
	s_lshl_b64 s[74:75], s[72:73], 20
	v_readlane_b32 s0, v255, 22
	v_ashrrev_i32_e32 v153, 31, v152
	s_add_u32 s74, s0, s74
	v_readlane_b32 s0, v255, 23
	s_addc_u32 s75, s0, s75
	v_lshlrev_b64 v[2:3], 7, v[152:153]
	v_lshl_add_u64 v[2:3], s[74:75], 0, v[2:3]
	v_lshl_add_u64 v[2:3], v[2:3], 0, v[162:163]
	global_load_dwordx4 v[126:129], v[2:3], off
	global_load_dwordx4 v[122:125], v[2:3], off offset:32
	global_load_dwordx4 v[118:121], v[2:3], off offset:64
	global_load_dwordx4 v[114:117], v[2:3], off offset:96
	v_add_u32_e32 v2, v178, v200
	s_barrier
	s_waitcnt vmcnt(15)
	ds_write_b128 v210, v[66:69]
	s_waitcnt vmcnt(14)
	ds_write_b128 v2, v[70:73] offset:49152
	s_waitcnt vmcnt(13)
	ds_write_b128 v211, v[74:77]
	v_add_u32_e32 v2, v178, v201
	s_waitcnt vmcnt(12)
	ds_write_b128 v2, v[78:81] offset:49152
	s_waitcnt vmcnt(11)
	ds_write_b128 v212, v[82:85]
	v_add_u32_e32 v2, v178, v202
	s_waitcnt vmcnt(10)
	ds_write_b128 v2, v[86:89] offset:49152
	s_waitcnt vmcnt(9)
	ds_write_b128 v213, v[90:93]
	v_add_u32_e32 v2, v178, v203
	s_waitcnt vmcnt(8)
	ds_write_b128 v2, v[94:97] offset:49152
	s_waitcnt vmcnt(7)
	ds_write_b128 v214, v[98:101]
	v_add_u32_e32 v2, v178, v204
	s_and_b32 s83, s83, 7
	s_waitcnt vmcnt(6)
	ds_write_b128 v2, v[102:105] offset:49152
	s_waitcnt vmcnt(5)
	ds_write_b128 v215, v[106:109]
	v_add_u32_e32 v2, v178, v205
	s_add_i32 s73, s83, 1
	s_waitcnt vmcnt(4)
	ds_write_b128 v2, v[110:113] offset:49152
	v_cvt_f32_ubyte0_e32 v2, s73
	s_mov_b32 s73, 0x42fc0000
	v_cmp_lt_f32_e32 vcc, s73, v2
	s_and_b64 s[74:75], vcc, exec
	s_cselect_b32 s73, 0xffffffc0, 0
	v_cndmask_b32_e32 v3, 0, v196, vcc
	v_sub_f32_e32 v2, v3, v2
	v_exp_f32_e32 v2, v2
	s_sub_i32 s84, s81, 64
	s_waitcnt lgkmcnt(0)
	s_barrier
	ds_read_b128 v[134:137], v227
	ds_read_b128 v[138:141], v228
	ds_read_b128 v[142:145], v229
	ds_read_b128 v[146:149], v230
	ds_read_b128 v[244:247], v227 offset:4096
	v_ldexp_f32 v2, v2, s73
	s_lshl_b32 s73, 1, s33
	v_cvt_f32_u32_e32 v3, s73
	s_lshr_b32 s73, 0x2000, s33
	s_cmp_gt_i32 s81, 63
	s_cselect_b64 s[74:75], -1, 0
	s_cmp_lt_i32 s84, s73
	s_cselect_b64 s[94:95], -1, 0
	v_mul_f32_e32 v2, v2, v3
	s_and_b64 s[74:75], s[74:75], s[94:95]
	v_mul_f32_e32 v154, 0x3fb8aa3b, v2
	v_cndmask_b32_e64 v2, v197, 0, s[74:75]
	s_mov_b32 s74, 0xc2800000
	v_fma_f32 v232, v154, s74, -v167
	v_add_f32_e32 v2, v232, v2
	s_mov_b32 s10, 0x41d00000
	s_mov_b32 s8, 0x41c00000
	s_mov_b32 s6, 0x41900000
	s_mov_b32 s96, 0x41800000
	s_mov_b32 s4, 0x41200000
	s_mov_b32 s76, 0x41000000
	s_mov_b32 s88, 2.0
	v_readlane_b32 s0, v254, 59
	v_fmac_f32_e32 v2, v154, v168
	s_mov_b32 s11, 0x41d80000
	s_mov_b32 s9, 0x41c80000
	s_mov_b32 s7, 0x41980000
	s_mov_b32 s97, 0x41880000
	s_mov_b32 s5, 0x41300000
	s_mov_b32 s77, 0x41100000
	s_mov_b32 s89, 0x40400000
	v_readlane_b32 s1, v254, 60
	v_pk_fma_f32 v[16:17], v[154:155], s[10:11], v[2:3] op_sel_hi:[0,1,0]
	v_pk_fma_f32 v[14:15], v[154:155], s[8:9], v[2:3] op_sel_hi:[0,1,0]
	v_pk_fma_f32 v[12:13], v[154:155], s[6:7], v[2:3] op_sel_hi:[0,1,0]
	v_pk_fma_f32 v[10:11], v[154:155], s[96:97], v[2:3] op_sel_hi:[0,1,0]
	v_pk_fma_f32 v[8:9], v[154:155], s[4:5], v[2:3] op_sel_hi:[0,1,0]
	v_pk_fma_f32 v[6:7], v[154:155], s[76:77], v[2:3] op_sel_hi:[0,1,0]
	v_pk_fma_f32 v[4:5], v[154:155], s[88:89], v[2:3] op_sel_hi:[0,1,0]
	v_pk_fma_f32 v[2:3], v[154:155], s[0:1], v[2:3] op_sel_hi:[0,1,0]
	s_add_i32 s79, s79, s87
	s_sub_i32 s84, s81, 32
	s_waitcnt vmcnt(3) lgkmcnt(4)
	v_mfma_f32_32x32x16_bf16 v[2:17], v[134:137], v[126:129], v[2:17]
	ds_read_b128 v[248:251], v228 offset:4096
	s_cmp_gt_i32 s81, 31
	s_cselect_b64 s[74:75], -1, 0
	s_cmp_lt_i32 s84, s73
	s_cselect_b64 s[94:95], -1, 0
	s_and_b64 s[74:75], s[74:75], s[94:95]
	s_cmpk_gt_i32 s79, 0x17ff
	s_waitcnt vmcnt(2) lgkmcnt(4)
	v_mfma_f32_32x32x16_bf16 v[2:17], v[138:141], v[122:125], v[2:17]
	ds_read_b128 v[134:137], v229 offset:4096
	s_waitcnt vmcnt(1) lgkmcnt(4)
	v_mfma_f32_32x32x16_bf16 v[2:17], v[142:145], v[118:121], v[2:17]
	ds_read_b128 v[138:141], v230 offset:4096
	s_waitcnt vmcnt(0) lgkmcnt(4)
	v_mfma_f32_32x32x16_bf16 v[2:17], v[146:149], v[114:117], v[2:17]
	ds_read_b64_tr_b16 v[142:143], v252 offset:45056
	ds_read_b64_tr_b16 v[144:145], v252 offset:46080
	v_cndmask_b32_e64 v18, v197, 0, s[74:75]
	s_mov_b32 s74, 0xc2000000
	v_fma_f32 v233, v154, s74, -v167
	v_add_f32_e32 v18, v233, v18
	v_fmac_f32_e32 v18, v154, v168
	v_pk_fma_f32 v[48:49], v[154:155], s[10:11], v[18:19] op_sel_hi:[0,1,0]
	v_pk_fma_f32 v[46:47], v[154:155], s[8:9], v[18:19] op_sel_hi:[0,1,0]
	v_pk_fma_f32 v[44:45], v[154:155], s[6:7], v[18:19] op_sel_hi:[0,1,0]
	v_pk_fma_f32 v[42:43], v[154:155], s[96:97], v[18:19] op_sel_hi:[0,1,0]
	v_pk_fma_f32 v[40:41], v[154:155], s[4:5], v[18:19] op_sel_hi:[0,1,0]
	v_pk_fma_f32 v[38:39], v[154:155], s[76:77], v[18:19] op_sel_hi:[0,1,0]
	v_pk_fma_f32 v[36:37], v[154:155], s[88:89], v[18:19] op_sel_hi:[0,1,0]
	v_pk_fma_f32 v[34:35], v[154:155], s[0:1], v[18:19] op_sel_hi:[0,1,0]
	s_waitcnt lgkmcnt(5)
	v_mfma_f32_32x32x16_bf16 v[34:49], v[244:247], v[126:129], v[34:49]
	ds_read_b64_tr_b16 v[146:147], v253 offset:45056
	ds_read_b64_tr_b16 v[148:149], v253 offset:46080
	s_waitcnt lgkmcnt(6)
	v_mfma_f32_32x32x16_bf16 v[34:49], v[248:251], v[122:125], v[34:49]
	ds_read_b64_tr_b16 v[244:245], v252 offset:47104
	ds_read_b64_tr_b16 v[246:247], v252 offset:48128
	s_waitcnt lgkmcnt(7)
	v_mfma_f32_32x32x16_bf16 v[34:49], v[134:137], v[118:121], v[34:49]
	ds_read_b64_tr_b16 v[248:249], v253 offset:47104
	ds_read_b64_tr_b16 v[250:251], v253 offset:48128
	s_waitcnt lgkmcnt(8)
	v_mfma_f32_32x32x16_bf16 v[34:49], v[138:141], v[114:117], v[34:49]
	ds_read_b128 v[134:137], v227 offset:8192
	s_cbranch_scc1 .LBB0_408
	s_ashr_i32 s84, s79, 8
	s_mul_hi_i32 s75, s84, 0x55555556
	s_add_i32 s74, s3, s71
	s_lshr_b32 s93, s75, 31
	s_and_b32 s74, s74, 56
	s_add_i32 s93, s75, s93
	s_add_i32 s74, s74, s93
	s_ashr_i32 s75, s74, 31
	s_lshl_b64 s[74:75], s[74:75], 20
	s_mul_i32 s93, s93, 3
	v_lshl_add_u64 v[18:19], v[132:133], 0, s[74:75]
	v_lshl_add_u64 v[20:21], v[130:131], 0, s[74:75]
	s_sub_i32 s74, s84, s93
	s_lshl_b32 s74, s74, 1
	s_lshr_b32 s84, 32, s74
	s_add_i32 s84, s84, -1
	s_bfe_u32 s93, s79, 0x50003
	s_and_b32 s84, s84, s93
	s_lshl_b32 s84, s84, 8
	s_lshr_b32 s75, 0x2000, s74
	s_sub_i32 s84, s84, 64
	s_add_i32 s75, s75, -1
	v_add_u32_e32 v22, s84, v172
	v_min_i32_e32 v23, s75, v22
	v_cmp_lt_i32_e32 vcc, -1, v22
	s_sub_i32 s94, 5, s74
	s_lshr_b32 s93, s93, s94
	v_cndmask_b32_e32 v22, 0, v23, vcc
	v_lshlrev_b32_e32 v22, s74, v22
	v_add_u32_e32 v22, s93, v22
	v_ashrrev_i32_e32 v23, 31, v22
	v_lshlrev_b64 v[22:23], 7, v[22:23]
	v_lshl_add_u64 v[24:25], v[20:21], 0, v[22:23]
	v_lshl_add_u64 v[22:23], v[18:19], 0, v[22:23]
	global_load_dwordx4 v[66:69], v[24:25], off
	global_load_dwordx4 v[70:73], v[22:23], off
	v_add_u32_e32 v22, s84, v173
	v_min_i32_e32 v23, s75, v22
	v_cmp_lt_i32_e32 vcc, -1, v22
	s_nop 1
	v_cndmask_b32_e32 v22, 0, v23, vcc
	v_lshlrev_b32_e32 v22, s74, v22
	v_add_u32_e32 v22, s93, v22
	v_ashrrev_i32_e32 v23, 31, v22
	v_lshlrev_b64 v[22:23], 7, v[22:23]
	v_lshl_add_u64 v[24:25], v[20:21], 0, v[22:23]
	v_lshl_add_u64 v[22:23], v[18:19], 0, v[22:23]
	global_load_dwordx4 v[74:77], v[24:25], off
	global_load_dwordx4 v[78:81], v[22:23], off
	v_add_u32_e32 v22, s84, v174
	v_min_i32_e32 v23, s75, v22
	v_cmp_lt_i32_e32 vcc, -1, v22
	s_nop 1
	v_cndmask_b32_e32 v22, 0, v23, vcc
	v_lshlrev_b32_e32 v22, s74, v22
	v_add_u32_e32 v22, s93, v22
	v_ashrrev_i32_e32 v23, 31, v22
	v_lshlrev_b64 v[22:23], 7, v[22:23]
	v_lshl_add_u64 v[24:25], v[20:21], 0, v[22:23]
	v_lshl_add_u64 v[22:23], v[18:19], 0, v[22:23]
	global_load_dwordx4 v[82:85], v[24:25], off
	global_load_dwordx4 v[86:89], v[22:23], off
	v_add_u32_e32 v22, s84, v175
	v_min_i32_e32 v23, s75, v22
	v_cmp_lt_i32_e32 vcc, -1, v22
	s_nop 1
	v_cndmask_b32_e32 v22, 0, v23, vcc
	v_lshlrev_b32_e32 v22, s74, v22
	v_add_u32_e32 v22, s93, v22
	v_ashrrev_i32_e32 v23, 31, v22
	v_lshlrev_b64 v[22:23], 7, v[22:23]
	v_lshl_add_u64 v[24:25], v[20:21], 0, v[22:23]
	v_lshl_add_u64 v[22:23], v[18:19], 0, v[22:23]
	global_load_dwordx4 v[90:93], v[24:25], off
	global_load_dwordx4 v[94:97], v[22:23], off
	v_add_u32_e32 v22, s84, v176
	v_min_i32_e32 v23, s75, v22
	v_cmp_lt_i32_e32 vcc, -1, v22
	s_nop 1
	v_cndmask_b32_e32 v22, 0, v23, vcc
	v_lshlrev_b32_e32 v22, s74, v22
	v_add_u32_e32 v22, s93, v22
	v_ashrrev_i32_e32 v23, 31, v22
	v_lshlrev_b64 v[22:23], 7, v[22:23]
	v_lshl_add_u64 v[24:25], v[20:21], 0, v[22:23]
	v_lshl_add_u64 v[22:23], v[18:19], 0, v[22:23]
	global_load_dwordx4 v[98:101], v[24:25], off
	global_load_dwordx4 v[102:105], v[22:23], off
	v_add_u32_e32 v22, s84, v177
	v_min_i32_e32 v23, s75, v22
	v_cmp_lt_i32_e32 vcc, -1, v22
	s_nop 1
	v_cndmask_b32_e32 v22, 0, v23, vcc
	v_lshlrev_b32_e32 v22, s74, v22
	v_add_u32_e32 v22, s93, v22
	v_ashrrev_i32_e32 v23, 31, v22
	v_lshlrev_b64 v[22:23], 7, v[22:23]
	v_lshl_add_u64 v[20:21], v[20:21], 0, v[22:23]
	v_lshl_add_u64 v[18:19], v[18:19], 0, v[22:23]
	global_load_dwordx4 v[106:109], v[20:21], off
	global_load_dwordx4 v[110:113], v[18:19], off
.LBB0_408:
	v_readlane_b32 s0, v255, 30
	v_readlane_b32 s1, v255, 31
	v_add_u32_e32 v231, 0, v171
	v_add_u32_e32 v151, 0, v169
	v_cndmask_b32_e64 v2, v197, v2, s[0:1]
	v_readlane_b32 s0, v255, 32
	v_readlane_b32 s1, v255, 33
	v_exp_f32_e32 v58, v2
	s_cmp_gt_i32 s81, -1
	v_cndmask_b32_e64 v3, v197, v3, s[0:1]
	v_readlane_b32 s0, v255, 34
	v_readlane_b32 s1, v255, 35
	v_exp_f32_e32 v59, v3
	s_cselect_b64 s[74:75], -1, 0
	v_cndmask_b32_e64 v2, v197, v4, s[0:1]
	v_readlane_b32 s0, v255, 36
	v_readlane_b32 s1, v255, 37
	v_exp_f32_e32 v60, v2
	v_cndmask_b32_e64 v2, v197, v6, s[12:13]
	v_cndmask_b32_e64 v3, v197, v5, s[0:1]
	v_exp_f32_e32 v61, v3
	v_cndmask_b32_e64 v3, v197, v7, s[14:15]
	v_exp_f32_e32 v62, v2
	v_exp_f32_e32 v63, v3
	v_cndmask_b32_e64 v2, v197, v8, s[16:17]
	v_cndmask_b32_e64 v3, v197, v9, s[18:19]
	v_exp_f32_e32 v64, v2
	v_exp_f32_e32 v65, v3
	v_cndmask_b32_e64 v2, v197, v10, s[20:21]
	v_cndmask_b32_e64 v3, v197, v11, s[22:23]
	v_exp_f32_e32 v156, v2
	v_exp_f32_e32 v157, v3
	v_cndmask_b32_e64 v2, v197, v12, s[24:25]
	v_cndmask_b32_e64 v3, v197, v13, s[26:27]
	v_exp_f32_e32 v236, v2
	v_exp_f32_e32 v237, v3
	v_cndmask_b32_e64 v2, v197, v14, s[28:29]
	v_cndmask_b32_e64 v3, v197, v15, s[30:31]
	v_exp_f32_e32 v238, v2
	v_exp_f32_e32 v239, v3
	v_cndmask_b32_e64 v2, v197, v16, s[34:35]
	v_cndmask_b32_e64 v3, v197, v17, s[36:37]
	v_exp_f32_e32 v240, v2
	v_exp_f32_e32 v241, v3
	v_cvt_pk_bf16_f32 v2, v58, v59
	v_cvt_pk_bf16_f32 v3, v60, v61
	v_cvt_pk_bf16_f32 v4, v62, v63
	v_cvt_pk_bf16_f32 v5, v64, v65
	v_cvt_pk_bf16_f32 v50, v156, v157
	v_cvt_pk_bf16_f32 v51, v236, v237
	s_waitcnt lgkmcnt(7)
	v_mfma_f32_32x32x16_bf16 v[18:33], v[142:145], v[2:5], 0
	ds_read_b128 v[138:141], v228 offset:8192
	v_cvt_pk_bf16_f32 v52, v238, v239
	v_cvt_pk_bf16_f32 v53, v240, v241
	s_cmp_lt_i32 s81, s73
	s_cselect_b64 s[94:95], -1, 0
	s_and_b64 s[74:75], s[74:75], s[94:95]
	s_waitcnt lgkmcnt(6)
	v_mfma_f32_32x32x16_bf16 v[2:17], v[146:149], v[2:5], 0
	ds_read_b128 v[142:145], v229 offset:8192
	v_exp_f32_e32 v242, v40
	v_exp_f32_e32 v243, v41
	v_exp_f32_e32 v42, v42
	v_exp_f32_e32 v43, v43
	v_exp_f32_e32 v44, v44
	v_exp_f32_e32 v45, v45
	v_exp_f32_e32 v46, v46
	s_waitcnt lgkmcnt(5)
	v_mfma_f32_32x32x16_bf16 v[18:33], v[244:247], v[50:53], v[18:33]
	ds_read_b128 v[146:149], v230 offset:8192
	v_exp_f32_e32 v47, v47
	v_exp_f32_e32 v48, v48
	v_exp_f32_e32 v49, v49
	s_add_i32 s84, s81, 32
	s_cmpk_gt_i32 s81, 0xffdf
	v_mul_f32_e32 v234, v154, v168
	s_waitcnt lgkmcnt(4)
	v_mfma_f32_32x32x16_bf16 v[2:17], v[248:251], v[50:53], v[2:17]
	ds_read_b64_tr_b16 v[244:245], v252 offset:49152
	ds_read_b64_tr_b16 v[246:247], v252 offset:50176
	v_add_f32_e64 v50, v58, 0
	v_add_f32_e64 v51, v59, 0
	v_readlane_b32 s0, v254, 59
	v_add_f32_e64 v50, v60, v50
	v_add_f32_e64 v51, v61, v51
	v_readlane_b32 s1, v254, 60
	v_pk_add_f32 v[50:51], v[62:63], v[50:51]
	s_nop 0
	v_pk_add_f32 v[50:51], v[64:65], v[50:51]
	s_nop 0
	v_pk_add_f32 v[50:51], v[156:157], v[50:51]
	s_nop 0
	v_pk_add_f32 v[50:51], v[236:237], v[50:51]
	s_nop 0
	v_pk_add_f32 v[50:51], v[238:239], v[50:51]
	v_pk_add_f32 v[156:157], v[240:241], v[50:51]
	v_cndmask_b32_e64 v235, v197, 0, s[74:75]
	v_fma_f32 v51, v154, 0, -v167
	v_add_f32_e32 v235, v51, v235
	v_mov_b32_e32 v50, v168
	v_add_f32_e32 v51, 1.0, v168
	v_add_f32_e32 v52, 2.0, v168
	v_add_f32_e32 v53, 0x40400000, v168
	v_add_f32_e32 v54, 0x41000000, v168
	v_add_f32_e32 v55, 0x41100000, v168
	v_add_f32_e32 v56, 0x41200000, v168
	v_add_f32_e32 v57, 0x41300000, v168
	v_add_f32_e32 v58, 0x41800000, v168
	v_add_f32_e32 v59, 0x41880000, v168
	v_add_f32_e32 v60, 0x41900000, v168
	v_add_f32_e32 v61, 0x41980000, v168
	v_add_f32_e32 v62, 0x41c00000, v168
	v_add_f32_e32 v63, 0x41c80000, v168
	v_add_f32_e32 v64, 0x41d00000, v168
	v_add_f32_e32 v65, 0x41d80000, v168
	v_fma_f32 v50, |v50|, -v154, v235
	v_fma_f32 v51, |v51|, -v154, v235
	v_fma_f32 v52, |v52|, -v154, v235
	v_fma_f32 v53, |v53|, -v154, v235
	v_fma_f32 v54, |v54|, -v154, v235
	v_fma_f32 v55, |v55|, -v154, v235
	v_fma_f32 v56, |v56|, -v154, v235
	v_fma_f32 v57, |v57|, -v154, v235
	v_fma_f32 v58, |v58|, -v154, v235
	v_fma_f32 v59, |v59|, -v154, v235
	v_fma_f32 v60, |v60|, -v154, v235
	v_fma_f32 v61, |v61|, -v154, v235
	v_fma_f32 v62, |v62|, -v154, v235
	v_fma_f32 v63, |v63|, -v154, v235
	v_fma_f32 v64, |v64|, -v154, v235
	v_fma_f32 v65, |v65|, -v154, v235
	v_exp_f32_e32 v240, v38
	v_exp_f32_e32 v241, v39
	s_waitcnt lgkmcnt(5)
	v_mfma_f32_32x32x16_bf16 v[50:65], v[134:137], v[126:129], v[50:65]
	ds_read_b64_tr_b16 v[248:249], v253 offset:49152
	ds_read_b64_tr_b16 v[250:251], v253 offset:50176
	s_cselect_b64 s[74:75], -1, 0
	s_cmp_lt_i32 s84, s73
	s_cselect_b64 s[94:95], -1, 0
	s_and_b64 s[74:75], s[74:75], s[94:95]
	s_add_i32 s84, s81, 64
	s_cmpk_gt_i32 s81, 0xffbf
	s_waitcnt lgkmcnt(6)
	v_mfma_f32_32x32x16_bf16 v[50:65], v[138:141], v[122:125], v[50:65]
	ds_read_b64_tr_b16 v[134:135], v252 offset:51200
	ds_read_b64_tr_b16 v[136:137], v252 offset:52224
	s_waitcnt lgkmcnt(7)
	v_mfma_f32_32x32x16_bf16 v[50:65], v[142:145], v[118:121], v[50:65]
	ds_read_b64_tr_b16 v[138:139], v253 offset:51200
	ds_read_b64_tr_b16 v[140:141], v253 offset:52224
	s_waitcnt lgkmcnt(8)
	v_mfma_f32_32x32x16_bf16 v[50:65], v[146:149], v[114:117], v[50:65]
	ds_read_b128 v[142:145], v227 offset:12288
	v_exp_f32_e32 v236, v34
	v_exp_f32_e32 v237, v35
	v_exp_f32_e32 v238, v36
	v_exp_f32_e32 v239, v37
	v_cvt_pk_bf16_f32 v36, v240, v241
	v_cvt_pk_bf16_f32 v34, v236, v237
	v_cvt_pk_bf16_f32 v37, v242, v243
	v_cvt_pk_bf16_f32 v35, v238, v239
	s_nop 3
	v_exp_f32_e32 v58, v58
	v_exp_f32_e32 v59, v59
	s_waitcnt lgkmcnt(7)
	v_mfma_f32_32x32x16_bf16 v[18:33], v[244:247], v[34:37], v[18:33]
	ds_read_b128 v[146:149], v228 offset:12288
	v_exp_f32_e32 v60, v60
	v_exp_f32_e32 v61, v61
	v_exp_f32_e32 v62, v62
	v_exp_f32_e32 v63, v63
	v_exp_f32_e32 v64, v64
	v_exp_f32_e32 v65, v65
	s_waitcnt lgkmcnt(6)
	v_mfma_f32_32x32x16_bf16 v[2:17], v[248:251], v[34:37], v[2:17]
	ds_read_b128 v[244:247], v229 offset:12288
	v_cvt_pk_bf16_f32 v34, v42, v43
	v_cvt_pk_bf16_f32 v35, v44, v45
	v_cvt_pk_bf16_f32 v36, v46, v47
	v_cvt_pk_bf16_f32 v37, v48, v49
	s_waitcnt lgkmcnt(5)
	s_nop 0
	v_mfma_f32_32x32x16_bf16 v[18:33], v[134:137], v[34:37], v[18:33]
	ds_read_b128 v[248:251], v230 offset:12288
	s_waitcnt lgkmcnt(4)
	v_mfma_f32_32x32x16_bf16 v[2:17], v[138:141], v[34:37], v[2:17]
	ds_read_b64_tr_b16 v[134:135], v252 offset:53248
	ds_read_b64_tr_b16 v[136:137], v252 offset:54272
	v_add_f32_e64 v34, v236, v156
	v_add_f32_e64 v35, v237, v157
	v_add_f32_e64 v34, v238, v34
	v_add_f32_e64 v35, v239, v35
	v_pk_add_f32 v[34:35], v[240:241], v[34:35]
	v_exp_f32_e32 v240, v54
	v_pk_add_f32 v[34:35], v[242:243], v[34:35]
	v_exp_f32_e32 v241, v55
	v_pk_add_f32 v[34:35], v[42:43], v[34:35]
	v_exp_f32_e32 v242, v56
	v_pk_add_f32 v[34:35], v[44:45], v[34:35]
	v_exp_f32_e32 v243, v57
	v_pk_add_f32 v[34:35], v[46:47], v[34:35]
	s_nop 0
	v_pk_add_f32 v[156:157], v[48:49], v[34:35]
	v_cndmask_b32_e64 v34, v197, 0, s[74:75]
	v_add_f32_e32 v34, v233, v34
	v_sub_f32_e32 v34, v34, v234
	v_pk_fma_f32 v[48:49], v[154:155], s[10:11], v[34:35] op_sel_hi:[0,1,0] neg_lo:[1,0,0] neg_hi:[1,0,0]
	v_pk_fma_f32 v[46:47], v[154:155], s[8:9], v[34:35] op_sel_hi:[0,1,0] neg_lo:[1,0,0] neg_hi:[1,0,0]
	v_pk_fma_f32 v[44:45], v[154:155], s[6:7], v[34:35] op_sel_hi:[0,1,0] neg_lo:[1,0,0] neg_hi:[1,0,0]
	v_pk_fma_f32 v[42:43], v[154:155], s[96:97], v[34:35] op_sel_hi:[0,1,0] neg_lo:[1,0,0] neg_hi:[1,0,0]
	v_pk_fma_f32 v[40:41], v[154:155], s[4:5], v[34:35] op_sel_hi:[0,1,0] neg_lo:[1,0,0] neg_hi:[1,0,0]
	v_pk_fma_f32 v[38:39], v[154:155], s[76:77], v[34:35] op_sel_hi:[0,1,0] neg_lo:[1,0,0] neg_hi:[1,0,0]
	v_pk_fma_f32 v[36:37], v[154:155], s[88:89], v[34:35] op_sel_hi:[0,1,0] neg_lo:[1,0,0] neg_hi:[1,0,0]
	v_pk_fma_f32 v[34:35], v[154:155], s[0:1], v[34:35] op_sel_hi:[0,1,0] neg_lo:[1,0,0] neg_hi:[1,0,0]
	s_cselect_b64 s[74:75], -1, 0
	s_cmp_lt_i32 s84, s73
	s_waitcnt lgkmcnt(5)
	v_mfma_f32_32x32x16_bf16 v[34:49], v[142:145], v[126:129], v[34:49]
	ds_read_b64_tr_b16 v[138:139], v253 offset:53248
	ds_read_b64_tr_b16 v[140:141], v253 offset:54272
	s_cselect_b64 s[94:95], -1, 0
	s_and_b64 s[74:75], s[74:75], s[94:95]
	s_add_i32 s73, 0, 0x10000
	s_waitcnt lgkmcnt(6)
	v_mfma_f32_32x32x16_bf16 v[34:49], v[146:149], v[122:125], v[34:49]
	ds_read_b64_tr_b16 v[142:143], v252 offset:55296
	ds_read_b64_tr_b16 v[144:145], v252 offset:56320
	s_waitcnt lgkmcnt(7)
	v_mfma_f32_32x32x16_bf16 v[34:49], v[244:247], v[118:121], v[34:49]
	ds_read_b64_tr_b16 v[146:147], v253 offset:55296
	ds_read_b64_tr_b16 v[148:149], v253 offset:56320
	s_waitcnt lgkmcnt(8)
	v_mfma_f32_32x32x16_bf16 v[34:49], v[248:251], v[114:117], v[34:49]
	ds_read_b128 v[244:247], v227 offset:16384
	v_exp_f32_e32 v236, v50
	v_exp_f32_e32 v237, v51
	v_exp_f32_e32 v238, v52
	v_exp_f32_e32 v239, v53
	v_cvt_pk_bf16_f32 v52, v240, v241
	v_cvt_pk_bf16_f32 v50, v236, v237
	v_cvt_pk_bf16_f32 v53, v242, v243
	v_cvt_pk_bf16_f32 v51, v238, v239
	s_nop 3
	v_exp_f32_e32 v34, v34
	v_exp_f32_e32 v35, v35
	s_waitcnt lgkmcnt(7)
	v_mfma_f32_32x32x16_bf16 v[18:33], v[134:137], v[50:53], v[18:33]
	ds_read_b128 v[248:251], v228 offset:16384
	v_exp_f32_e32 v36, v36
	v_exp_f32_e32 v37, v37
	v_exp_f32_e32 v38, v38
	v_exp_f32_e32 v39, v39
	v_exp_f32_e32 v40, v40
	v_exp_f32_e32 v41, v41
	s_waitcnt lgkmcnt(6)
	v_mfma_f32_32x32x16_bf16 v[2:17], v[138:141], v[50:53], v[2:17]
	ds_read_b128 v[134:137], v229 offset:16384
	v_cvt_pk_bf16_f32 v50, v58, v59
	v_cvt_pk_bf16_f32 v51, v60, v61
	v_cvt_pk_bf16_f32 v52, v62, v63
	v_cvt_pk_bf16_f32 v53, v64, v65
	v_exp_f32_e32 v42, v42
	v_exp_f32_e32 v43, v43
	s_waitcnt lgkmcnt(5)
	v_mfma_f32_32x32x16_bf16 v[18:33], v[142:145], v[50:53], v[18:33]
	ds_read_b128 v[138:141], v230 offset:16384
	v_exp_f32_e32 v44, v44
	v_exp_f32_e32 v45, v45
	s_waitcnt lgkmcnt(4)
	v_mfma_f32_32x32x16_bf16 v[2:17], v[146:149], v[50:53], v[2:17]
	ds_read_b64_tr_b16 v[142:143], v252 offset:57344
	ds_read_b64_tr_b16 v[144:145], v252 offset:58368
	v_add_f32_e64 v50, v156, v236
	v_add_f32_e64 v51, v157, v237
	v_add_f32_e64 v50, v238, v50
	v_add_f32_e64 v51, v239, v51
	v_add_f32_e64 v50, v240, v50
	v_add_f32_e64 v51, v241, v51
	v_pk_add_f32 v[50:51], v[242:243], v[50:51]
	s_nop 0
	v_pk_add_f32 v[50:51], v[58:59], v[50:51]
	s_nop 0
	v_pk_add_f32 v[50:51], v[60:61], v[50:51]
	s_nop 0
	v_pk_add_f32 v[50:51], v[62:63], v[50:51]
	s_nop 0
	v_pk_add_f32 v[156:157], v[64:65], v[50:51]
	v_cndmask_b32_e64 v50, v197, 0, s[74:75]
	v_add_f32_e32 v50, v232, v50
	v_sub_f32_e32 v50, v50, v234
	v_pk_fma_f32 v[64:65], v[154:155], s[10:11], v[50:51] op_sel_hi:[0,1,0] neg_lo:[1,0,0] neg_hi:[1,0,0]
	v_pk_fma_f32 v[62:63], v[154:155], s[8:9], v[50:51] op_sel_hi:[0,1,0] neg_lo:[1,0,0] neg_hi:[1,0,0]
	v_pk_fma_f32 v[60:61], v[154:155], s[6:7], v[50:51] op_sel_hi:[0,1,0] neg_lo:[1,0,0] neg_hi:[1,0,0]
	v_pk_fma_f32 v[58:59], v[154:155], s[96:97], v[50:51] op_sel_hi:[0,1,0] neg_lo:[1,0,0] neg_hi:[1,0,0]
	v_pk_fma_f32 v[56:57], v[154:155], s[4:5], v[50:51] op_sel_hi:[0,1,0] neg_lo:[1,0,0] neg_hi:[1,0,0]
	v_pk_fma_f32 v[54:55], v[154:155], s[76:77], v[50:51] op_sel_hi:[0,1,0] neg_lo:[1,0,0] neg_hi:[1,0,0]
	v_pk_fma_f32 v[52:53], v[154:155], s[88:89], v[50:51] op_sel_hi:[0,1,0] neg_lo:[1,0,0] neg_hi:[1,0,0]
	v_pk_fma_f32 v[50:51], v[154:155], s[0:1], v[50:51] op_sel_hi:[0,1,0] neg_lo:[1,0,0] neg_hi:[1,0,0]
	v_readlane_b32 s0, v254, 61
	s_waitcnt lgkmcnt(5)
	v_mfma_f32_32x32x16_bf16 v[50:65], v[244:247], v[126:129], v[50:65]
	ds_read_b64_tr_b16 v[146:147], v253 offset:57344
	ds_read_b64_tr_b16 v[148:149], v253 offset:58368
	s_waitcnt lgkmcnt(6)
	v_mfma_f32_32x32x16_bf16 v[50:65], v[248:251], v[122:125], v[50:65]
	ds_read_b64_tr_b16 v[244:245], v252 offset:59392
	ds_read_b64_tr_b16 v[246:247], v252 offset:60416
	s_waitcnt lgkmcnt(7)
	v_mfma_f32_32x32x16_bf16 v[50:65], v[134:137], v[118:121], v[50:65]
	ds_read_b64_tr_b16 v[248:249], v253 offset:59392
	ds_read_b64_tr_b16 v[250:251], v253 offset:60416
	s_waitcnt lgkmcnt(8)
	v_mfma_f32_32x32x16_bf16 v[50:65], v[138:141], v[114:117], v[50:65]
	ds_read_b64_tr_b16 v[134:135], v252 offset:61440
	ds_read_b64_tr_b16 v[136:137], v252 offset:62464
	v_exp_f32_e32 v118, v46
	v_exp_f32_e32 v119, v47
	v_exp_f32_e32 v120, v48
	v_exp_f32_e32 v121, v49
	v_cvt_pk_bf16_f32 v46, v34, v35
	v_cvt_pk_bf16_f32 v47, v36, v37
	v_cvt_pk_bf16_f32 v48, v38, v39
	v_cvt_pk_bf16_f32 v49, v40, v41
	v_pk_add_f32 v[34:35], v[156:157], v[34:35]
	s_waitcnt lgkmcnt(8)
	v_mfma_f32_32x32x16_bf16 v[18:33], v[142:145], v[46:49], v[18:33]
	ds_read_b64_tr_b16 v[138:139], v253 offset:61440
	ds_read_b64_tr_b16 v[140:141], v253 offset:62464
	v_add_f32_e64 v34, v36, v34
	v_add_f32_e64 v35, v37, v35
	v_add_f32_e64 v34, v38, v34
	v_add_f32_e64 v35, v39, v35
	v_pk_add_f32 v[34:35], v[40:41], v[34:35]
	s_waitcnt lgkmcnt(8)
	v_mfma_f32_32x32x16_bf16 v[2:17], v[146:149], v[46:49], v[2:17]
	ds_read_b64_tr_b16 v[142:143], v252 offset:63488
	ds_read_b64_tr_b16 v[144:145], v252 offset:64512
	v_cvt_pk_bf16_f32 v46, v42, v43
	v_cvt_pk_bf16_f32 v47, v44, v45
	v_cvt_pk_bf16_f32 v48, v118, v119
	v_cvt_pk_bf16_f32 v49, v120, v121
	v_pk_add_f32 v[34:35], v[42:43], v[34:35]
	s_waitcnt lgkmcnt(8)
	v_mfma_f32_32x32x16_bf16 v[18:33], v[244:247], v[46:49], v[18:33]
	ds_read_b64_tr_b16 v[146:147], v253 offset:63488
	ds_read_b64_tr_b16 v[148:149], v253 offset:64512
	v_add_f32_e64 v34, v44, v34
	v_add_f32_e64 v35, v45, v35
	v_pk_add_f32 v[34:35], v[118:119], v[34:35]
	s_nop 0
	v_pk_add_f32 v[42:43], v[120:121], v[34:35]
	v_cndmask_b32_e64 v34, v197, v50, s[38:39]
	v_cndmask_b32_e64 v35, v197, v51, s[40:41]
	v_exp_f32_e32 v44, v34
	v_exp_f32_e32 v45, v35
	v_cndmask_b32_e64 v34, v197, v52, s[42:43]
	v_cndmask_b32_e64 v35, v197, v53, s[44:45]
	s_waitcnt lgkmcnt(8)
	v_mfma_f32_32x32x16_bf16 v[2:17], v[248:251], v[46:49], v[2:17]
	v_exp_f32_e32 v46, v34
	v_exp_f32_e32 v47, v35
	v_cndmask_b32_e64 v34, v197, v54, s[46:47]
	v_cndmask_b32_e64 v35, v197, v55, s[48:49]
	v_exp_f32_e32 v48, v34
	v_exp_f32_e32 v49, v35
	v_cndmask_b32_e64 v34, v197, v56, s[50:51]
	v_cndmask_b32_e64 v35, v197, v57, s[52:53]
	v_exp_f32_e32 v50, v34
	v_exp_f32_e32 v51, v35
	v_cndmask_b32_e64 v34, v197, v58, s[54:55]
	v_cndmask_b32_e64 v35, v197, v59, s[56:57]
	v_exp_f32_e32 v52, v34
	v_exp_f32_e32 v53, v35
	v_cndmask_b32_e64 v34, v197, v60, s[58:59]
	v_cndmask_b32_e64 v35, v197, v61, s[60:61]
	v_exp_f32_e32 v54, v34
	v_exp_f32_e32 v55, v35
	v_cndmask_b32_e64 v34, v197, v62, s[62:63]
	v_cndmask_b32_e64 v35, v197, v63, s[64:65]
	v_exp_f32_e32 v56, v34
	v_exp_f32_e32 v57, v35
	v_cndmask_b32_e64 v34, v197, v64, s[66:67]
	v_cndmask_b32_e64 v35, v197, v65, s[68:69]
	v_exp_f32_e32 v58, v34
	v_exp_f32_e32 v59, v35
	v_cvt_pk_bf16_f32 v34, v44, v45
	v_cvt_pk_bf16_f32 v35, v46, v47
	v_cvt_pk_bf16_f32 v36, v48, v49
	v_cvt_pk_bf16_f32 v37, v50, v51
	s_waitcnt lgkmcnt(6)
	s_nop 0
	v_mfma_f32_32x32x16_bf16 v[18:33], v[134:137], v[34:37], v[18:33]
	s_waitcnt lgkmcnt(4)
	v_mfma_f32_32x32x16_bf16 v[2:17], v[138:141], v[34:37], v[2:17]
	v_cvt_pk_bf16_f32 v34, v52, v53
	v_cvt_pk_bf16_f32 v35, v54, v55
	v_cvt_pk_bf16_f32 v36, v56, v57
	v_cvt_pk_bf16_f32 v37, v58, v59
	s_waitcnt lgkmcnt(2)
	s_nop 0
	v_mfma_f32_32x32x16_bf16 v[18:33], v[142:145], v[34:37], v[18:33]
	v_readlane_b32 s0, v255, 28
	v_readlane_b32 s1, v255, 29
	s_waitcnt lgkmcnt(0)
	v_mfma_f32_32x32x16_bf16 v[2:17], v[146:149], v[34:37], v[2:17]
	v_add_f32_e64 v34, v42, v44
	v_add_f32_e64 v35, v43, v45
	v_add_f32_e64 v34, v46, v34
	v_add_f32_e64 v35, v47, v35
	v_add_f32_e64 v34, v48, v34
	v_add_f32_e64 v35, v49, v35
	v_pk_add_f32 v[34:35], v[50:51], v[34:35]
	s_nop 0
	v_pk_add_f32 v[34:35], v[52:53], v[34:35]
	s_nop 0
	v_pk_add_f32 v[34:35], v[54:55], v[34:35]
	s_nop 0
	v_pk_add_f32 v[34:35], v[56:57], v[34:35]
	s_nop 0
	v_pk_add_f32 v[34:35], v[58:59], v[34:35]
	s_nop 0
	v_add_f32_e32 v34, v34, v35
	v_mov_b32_e32 v35, v34
	s_nop 1
	v_permlane32_swap_b32 v34, v35
	s_nop 0
	v_add_f32_e32 v34, v34, v35
	v_div_scale_f32 v35, s[74:75], v34, v34, 1.0
	v_rcp_f32_e32 v36, v35
	s_nop 0
	v_fma_f32 v37, -v35, v36, 1.0
	v_fmac_f32_e32 v36, v37, v36
	v_div_scale_f32 v37, vcc, 1.0, v34, 1.0
	v_mul_f32_e32 v38, v37, v36
	v_fma_f32 v39, -v35, v38, v37
	v_fmac_f32_e32 v38, v39, v36
	v_fma_f32 v35, -v35, v38, v37
	v_div_fmas_f32 v35, v35, v36, v38
	v_div_fixup_f32 v36, v35, v34, 1.0
	v_pk_mul_f32 v[18:19], v[18:19], v[36:37] op_sel_hi:[1,0]
	v_pk_mul_f32 v[20:21], v[20:21], v[36:37] op_sel_hi:[1,0]
	v_cvt_pk_bf16_f32 v18, v18, v19
	v_cvt_pk_bf16_f32 v19, v20, v21
	v_add_u32_e32 v20, v179, v206
	ds_write_b64 v20, v[18:19]
	v_pk_mul_f32 v[18:19], v[22:23], v[36:37] op_sel_hi:[1,0]
	v_pk_mul_f32 v[20:21], v[24:25], v[36:37] op_sel_hi:[1,0]
	v_cvt_pk_bf16_f32 v18, v18, v19
	v_cvt_pk_bf16_f32 v19, v20, v21
	ds_write_b64 v216, v[18:19]
	v_pk_mul_f32 v[18:19], v[26:27], v[36:37] op_sel_hi:[1,0]
	v_pk_mul_f32 v[20:21], v[28:29], v[36:37] op_sel_hi:[1,0]
	v_cvt_pk_bf16_f32 v18, v18, v19
	v_cvt_pk_bf16_f32 v19, v20, v21
	ds_write_b64 v217, v[18:19]
	v_pk_mul_f32 v[18:19], v[30:31], v[36:37] op_sel_hi:[1,0]
	v_pk_mul_f32 v[20:21], v[32:33], v[36:37] op_sel_hi:[1,0]
	v_pk_mul_f32 v[2:3], v[2:3], v[36:37] op_sel_hi:[1,0]
	v_pk_mul_f32 v[4:5], v[4:5], v[36:37] op_sel_hi:[1,0]
	v_cvt_pk_bf16_f32 v18, v18, v19
	v_cvt_pk_bf16_f32 v19, v20, v21
	v_cvt_pk_bf16_f32 v2, v2, v3
	v_cvt_pk_bf16_f32 v3, v4, v5
	ds_write_b64 v218, v[18:19]
	ds_write_b64 v219, v[2:3]
	v_pk_mul_f32 v[2:3], v[6:7], v[36:37] op_sel_hi:[1,0]
	v_pk_mul_f32 v[4:5], v[8:9], v[36:37] op_sel_hi:[1,0]
	v_cvt_pk_bf16_f32 v2, v2, v3
	v_cvt_pk_bf16_f32 v3, v4, v5
	ds_write_b64 v220, v[2:3]
	v_pk_mul_f32 v[2:3], v[10:11], v[36:37] op_sel_hi:[1,0]
	v_pk_mul_f32 v[4:5], v[12:13], v[36:37] op_sel_hi:[1,0]
	v_cvt_pk_bf16_f32 v2, v2, v3
	v_cvt_pk_bf16_f32 v3, v4, v5
	ds_write_b64 v221, v[2:3]
	v_pk_mul_f32 v[2:3], v[14:15], v[36:37] op_sel_hi:[1,0]
	v_pk_mul_f32 v[4:5], v[16:17], v[36:37] op_sel_hi:[1,0]
	v_cvt_pk_bf16_f32 v2, v2, v3
	v_cvt_pk_bf16_f32 v3, v4, v5
	ds_write_b64 v222, v[2:3]
	s_and_saveexec_b64 s[74:75], s[0:1]
	s_xor_b64 s[74:75], exec, s[74:75]
	s_ashr_i32 s93, s92, 31
	s_or_saveexec_b64 s[94:95], s[74:75]
	s_ashr_i32 s74, s72, 3
	s_ashr_i32 s75, s74, 31
	v_mov_b64_e32 v[2:3], s[92:93]
	s_mov_b32 s76, 0xfe5163ab
	s_mov_b32 s77, 0x3c439041
	s_mov_b32 s96, 0xdb629599
	s_mov_b32 s97, 0xf534ddc0
	s_xor_b64 exec, exec, s[94:95]
	s_cbranch_execz .LBB0_405
	s_mov_b32 s72, 0x800000
	v_cmp_gt_f32_e32 vcc, s72, v34
	s_mov_b32 s72, 0x3f317217
	s_ashr_i32 s93, s92, 31
	v_cndmask_b32_e64 v2, 0, 32, vcc
	v_ldexp_f32 v2, v34, v2
	v_log_f32_e32 v2, v2
	v_readlane_b32 s0, v255, 26
	v_mul_f32_e32 v3, 0x3f317217, v2
	v_fma_f32 v3, v2, s72, -v3
	v_fmac_f32_e32 v3, 0x3377d1cf, v2
	s_mov_b32 s72, 0x7f800000
	v_fmac_f32_e32 v3, 0x3f317217, v2
	v_cmp_lt_f32_e64 s[72:73], |v2|, s72
	s_nop 1
	v_cndmask_b32_e64 v2, v2, v3, s[72:73]
	s_lshl_b64 s[72:73], s[92:93], 21
	s_add_u32 s84, s0, s72
	v_readlane_b32 s0, v255, 27
	v_cndmask_b32_e32 v3, 0, v198, vcc
	s_addc_u32 vcc_lo, s0, s73
	s_lshl_b64 s[72:73], s[74:75], 18
	v_sub_f32_e32 v2, v2, v3
	s_add_u32 s72, s84, s72
	v_add_f32_e32 v4, v166, v2
	v_lshlrev_b64 v[2:3], 5, v[152:153]
	s_addc_u32 s73, vcc_lo, s73
	v_lshl_add_u64 v[2:3], s[72:73], 0, v[2:3]
	s_lshl_b32 s84, s83, 2
	v_lshl_add_u64 v[2:3], v[2:3], 0, s[84:85]
	global_store_dword v[2:3], v4, off
	v_mov_b64_e32 v[2:3], s[92:93]
	s_branch .LBB0_405
